# P7: half of the workgroups stream their two residual blocks into the memory-side cache while the other half runs its first K loop (doubles as the half-epilogue offset)
# speedup vs baseline: 1.0048x; 1.0048x over previous
;     __device__ __forceinline__ void init(const void* A_, int slabA_, const void* Bt_, size_t estride_bytes, int rowbytes, const LAS int* ts_, int nN_, int G_, int c_) { slabA = slabA_; A = (const char*)A_; Bt = (const char*)Bt_; estride = estride_bytes; rowb = rowbytes; ts = ts_; nN = nN_; nwg = __builtin_amdgcn_readfirstlane(ts_[NE]) * nN_; G = G_; c = c_; }
;     __device__ __forceinline__ void operator()(const f32x4 (&acc)[2][2][4][2], const Unit& u, int wr, int wc, int fr, int fq) const {
;     ...
;             for (int m = 0; m < 4; ++m) { const size_t off = (size_t)(row0 + ai * HALF + m * 16) * DM + col0;
; #pragma unroll
;                 for (int bj = 0; bj < 2; ++bj) { const f32x4 v0 = *(const f32x4*)(base + off + bj * HALF) + acc[ai][bj][m][0], v1 = *(const f32x4*)(base + off + bj * HALF + 4) + acc[ai][bj][m][1];
; __global__ void __launch_bounds__(512, 2) fwd_kernel(Params p) {
;     ...
;     if (IN(7)) {
;         pg8::DenseOrder S; S.init(MERGED, DM, WoutT, DM, T, DM, G, bx);
;         pg8::EpiOut E{p.in[I_X], X1, H2, p.in[I_GFFN]};
;         pg8::gemm_phase(lds, DM, DM, DM, S, E, wave);
.LBB0_901:
	s_or_b64 exec, exec, s[10:11]
	s_add_u32 s10, s28, 0x17800000
	s_addc_u32 s11, s29, 0
	s_add_u32 s14, s28, 0x9c000000
	s_addc_u32 s15, s29, 0
	s_andn2_b64 vcc, exec, s[6:7]
	s_waitcnt lgkmcnt(0)
	s_barrier
	v_mbcnt_lo_u32_b32 v0, -1, 0
	v_mbcnt_hi_u32_b32 v0, -1, v0
	s_cbranch_vccnz .LBB0_925
	s_cmpk_lg_i32 s33, 0x100
	s_cbranch_scc1 .Lp7_nopf
	s_bitcmp1_b32 s2, 6
	s_cbranch_scc0 .Lp7_nopf
	s_load_dwordx2 s[98:99], s[88:89], 0x0
	v_readlane_b32 s0, v252, 3
	s_and_b32 s3, s2, 7
	s_lshl_b32 s3, s3, 3
	s_bfe_u32 s8, s2, 0x30003
	s_add_i32 s3, s3, s8
	s_lshl_b32 s3, s3, 8
	s_lshr_b32 s0, s0, 1
	s_add_i32 s3, s3, s0
	s_lshl_b32 s3, s3, 13
	s_lshr_b32 s8, s2, 6
	s_lshl_b32 s8, s8, 10
	s_add_i32 s3, s3, s8
	v_lshlrev_b32_e32 v238, 4, v0
	v_add_u32_e32 v238, s3, v238
	v_add_u32_e32 v239, 0x1000, v238
	s_waitcnt lgkmcnt(0)
	global_load_dwordx4 v[234:237], v238, s[98:99]
	global_load_dwordx4 v[234:237], v239, s[98:99]
	v_add_u32_e32 v238, 0x2000, v238
	v_add_u32_e32 v239, 0x2000, v239
	global_load_dwordx4 v[234:237], v238, s[98:99]
	global_load_dwordx4 v[234:237], v239, s[98:99]
	v_add_u32_e32 v238, 0x2000, v238
	v_add_u32_e32 v239, 0x2000, v239
	global_load_dwordx4 v[234:237], v238, s[98:99]
	global_load_dwordx4 v[234:237], v239, s[98:99]
	v_add_u32_e32 v238, 0x2000, v238
	v_add_u32_e32 v239, 0x2000, v239
	global_load_dwordx4 v[234:237], v238, s[98:99]
	global_load_dwordx4 v[234:237], v239, s[98:99]
	v_add_u32_e32 v238, 0x2000, v238
	v_add_u32_e32 v239, 0x2000, v239
	global_load_dwordx4 v[234:237], v238, s[98:99]
	global_load_dwordx4 v[234:237], v239, s[98:99]
	v_add_u32_e32 v238, 0x2000, v238
	v_add_u32_e32 v239, 0x2000, v239
	global_load_dwordx4 v[234:237], v238, s[98:99]
	global_load_dwordx4 v[234:237], v239, s[98:99]
	v_add_u32_e32 v238, 0x2000, v238
	v_add_u32_e32 v239, 0x2000, v239
	global_load_dwordx4 v[234:237], v238, s[98:99]
	global_load_dwordx4 v[234:237], v239, s[98:99]
	v_add_u32_e32 v238, 0x2000, v238
	v_add_u32_e32 v239, 0x2000, v239
	global_load_dwordx4 v[234:237], v238, s[98:99]
	global_load_dwordx4 v[234:237], v239, s[98:99]
	v_add_u32_e32 v238, 0x2000, v238
	v_add_u32_e32 v239, 0x2000, v239
	global_load_dwordx4 v[234:237], v238, s[98:99]
	global_load_dwordx4 v[234:237], v239, s[98:99]
	v_add_u32_e32 v238, 0x2000, v238
	v_add_u32_e32 v239, 0x2000, v239
	global_load_dwordx4 v[234:237], v238, s[98:99]
	global_load_dwordx4 v[234:237], v239, s[98:99]
	v_add_u32_e32 v238, 0x2000, v238
	v_add_u32_e32 v239, 0x2000, v239
	global_load_dwordx4 v[234:237], v238, s[98:99]
	global_load_dwordx4 v[234:237], v239, s[98:99]
	v_add_u32_e32 v238, 0x2000, v238
	v_add_u32_e32 v239, 0x2000, v239
	global_load_dwordx4 v[234:237], v238, s[98:99]
	global_load_dwordx4 v[234:237], v239, s[98:99]
	v_add_u32_e32 v238, 0x2000, v238
	v_add_u32_e32 v239, 0x2000, v239
	global_load_dwordx4 v[234:237], v238, s[98:99]
	global_load_dwordx4 v[234:237], v239, s[98:99]
	v_add_u32_e32 v238, 0x2000, v238
	v_add_u32_e32 v239, 0x2000, v239
	global_load_dwordx4 v[234:237], v238, s[98:99]
	global_load_dwordx4 v[234:237], v239, s[98:99]
	v_add_u32_e32 v238, 0x2000, v238
	v_add_u32_e32 v239, 0x2000, v239
	global_load_dwordx4 v[234:237], v238, s[98:99]
	global_load_dwordx4 v[234:237], v239, s[98:99]
	v_add_u32_e32 v238, 0x2000, v238
	v_add_u32_e32 v239, 0x2000, v239
	global_load_dwordx4 v[234:237], v238, s[98:99]
	global_load_dwordx4 v[234:237], v239, s[98:99]
	v_add_u32_e32 v238, 0x2000, v238
	v_add_u32_e32 v239, 0x2000, v239
	global_load_dwordx4 v[234:237], v238, s[98:99]
	global_load_dwordx4 v[234:237], v239, s[98:99]
	v_add_u32_e32 v238, 0x2000, v238
	v_add_u32_e32 v239, 0x2000, v239
	global_load_dwordx4 v[234:237], v238, s[98:99]
	global_load_dwordx4 v[234:237], v239, s[98:99]
	v_add_u32_e32 v238, 0x2000, v238
	v_add_u32_e32 v239, 0x2000, v239
	global_load_dwordx4 v[234:237], v238, s[98:99]
	global_load_dwordx4 v[234:237], v239, s[98:99]
	v_add_u32_e32 v238, 0x2000, v238
	v_add_u32_e32 v239, 0x2000, v239
	global_load_dwordx4 v[234:237], v238, s[98:99]
	global_load_dwordx4 v[234:237], v239, s[98:99]
	v_add_u32_e32 v238, 0x2000, v238
	v_add_u32_e32 v239, 0x2000, v239
	global_load_dwordx4 v[234:237], v238, s[98:99]
	global_load_dwordx4 v[234:237], v239, s[98:99]
	v_add_u32_e32 v238, 0x2000, v238
	v_add_u32_e32 v239, 0x2000, v239
	global_load_dwordx4 v[234:237], v238, s[98:99]
	global_load_dwordx4 v[234:237], v239, s[98:99]
	v_add_u32_e32 v238, 0x2000, v238
	v_add_u32_e32 v239, 0x2000, v239
	global_load_dwordx4 v[234:237], v238, s[98:99]
	global_load_dwordx4 v[234:237], v239, s[98:99]
	v_add_u32_e32 v238, 0x2000, v238
	v_add_u32_e32 v239, 0x2000, v239
	global_load_dwordx4 v[234:237], v238, s[98:99]
	global_load_dwordx4 v[234:237], v239, s[98:99]
	v_add_u32_e32 v238, 0x2000, v238
	v_add_u32_e32 v239, 0x2000, v239
	global_load_dwordx4 v[234:237], v238, s[98:99]
	global_load_dwordx4 v[234:237], v239, s[98:99]
	v_add_u32_e32 v238, 0x2000, v238
	v_add_u32_e32 v239, 0x2000, v239
	global_load_dwordx4 v[234:237], v238, s[98:99]
	global_load_dwordx4 v[234:237], v239, s[98:99]
	v_add_u32_e32 v238, 0x2000, v238
	v_add_u32_e32 v239, 0x2000, v239
	global_load_dwordx4 v[234:237], v238, s[98:99]
	global_load_dwordx4 v[234:237], v239, s[98:99]
	v_add_u32_e32 v238, 0x2000, v238
	v_add_u32_e32 v239, 0x2000, v239
	global_load_dwordx4 v[234:237], v238, s[98:99]
	global_load_dwordx4 v[234:237], v239, s[98:99]
	v_add_u32_e32 v238, 0x2000, v238
	v_add_u32_e32 v239, 0x2000, v239
	global_load_dwordx4 v[234:237], v238, s[98:99]
	global_load_dwordx4 v[234:237], v239, s[98:99]
	v_add_u32_e32 v238, 0x2000, v238
	v_add_u32_e32 v239, 0x2000, v239
	global_load_dwordx4 v[234:237], v238, s[98:99]
	global_load_dwordx4 v[234:237], v239, s[98:99]
	v_add_u32_e32 v238, 0x2000, v238
	v_add_u32_e32 v239, 0x2000, v239
	global_load_dwordx4 v[234:237], v238, s[98:99]
	global_load_dwordx4 v[234:237], v239, s[98:99]
	v_add_u32_e32 v238, 0x2000, v238
	v_add_u32_e32 v239, 0x2000, v239
	global_load_dwordx4 v[234:237], v238, s[98:99]
	global_load_dwordx4 v[234:237], v239, s[98:99]
	s_waitcnt vmcnt(0)
